# strategy 8 continued: chain MFMA order changed so the output (Y) chain finishes two MFMAs earlier and its bf16 conversions issue in the shadow of the last state MFMAs
# baseline (speedup 1.0000x reference)
; #define LAS __attribute__((address_space(3)))
; DI unsigned cvt2(float lo, float hi) { return __builtin_bit_cast(unsigned, __builtin_convertvector((f32x2){lo, hi}, bfv2)); }
; DI void phase_chain(const Frame& F) {
;     ...
;             for (int jj = 0; jj < NSUB; ++jj) {
;                 __builtin_amdgcn_s_barrier(); asm volatile("" ::: "memory");
;                 const LAS unsigned char* st = ring + cur * CH_STB;
;                 bf16x8 sb[4]; sb[0] = pack8(S0, 0); sb[1] = pack8(S0, 1); sb[2] = pack8(S1, 0); sb[3] = pack8(S1, 1);
;                 const bf16x8 vt = *(const LAS bf16x8*)(st + 12800 + r * 32 + h * 16), wh = *(const LAS bf16x8*)(st + 12288 + rs * 32 + h * 16);
;                 const bf16x8 kh0 = *(const LAS bf16x8*)(st + 8192 + r * 32 + h * 16), kh1 = *(const LAS bf16x8*)(st + 8192 + (32 + r) * 32 + h * 16);
;                 f32x16 Y, N0, N1;
; #pragma unroll
;                 for (int i = 0; i < 16; ++i) { Y[i] = 0.f; N0[i] = 0.f; N1[i] = 0.f; }
;                 Y = __builtin_amdgcn_mfma_f32_32x32x16_bf16(wh, vt, Y, 0, 0, 0);
;                 N0 = __builtin_amdgcn_mfma_f32_32x32x16_bf16(kh0, vt, N0, 0, 0, 0);
;                 N1 = __builtin_amdgcn_mfma_f32_32x32x16_bf16(kh1, vt, N1, 0, 0, 0);
; #pragma unroll
;                 for (int ks = 0; ks < 4; ++ks) { const int c0 = ((4 * ks + h) ^ rs) * 8, c1 = ((4 * ks + h + 2) ^ rs) * 8;
;                     Y = __builtin_amdgcn_mfma_f32_32x32x16_bf16(cat8(st + 10240 + rs * 128 + c0, st + 10240 + rs * 128 + c1), sb[ks], Y, 0, 0, 0);
;                     N0 = __builtin_amdgcn_mfma_f32_32x32x16_bf16(cat8(st + r * 128 + c0, st + r * 128 + c1), sb[ks], N0, 0, 0, 0);
;                     N1 = __builtin_amdgcn_mfma_f32_32x32x16_bf16(cat8(st + (32 + r) * 128 + c0, st + (32 + r) * 128 + c1), sb[ks], N1, 0, 0, 0); }
;                 S0 = N0; S1 = N1;
; #pragma unroll
;                 for (int q = 0; q < 8; q += 1) { const int t = (q & 3) + 8 * (q >> 2) + 4 * h; *(LAS bf16_t*)(ybuf + (t * 32 + r) * 2) = (bf16_t)(cvt2(Y[q], 0.f) & 0xffffu); }
;                 { const u32x4 w = *(const LAS u32x4*)(ybuf + F.lane * 16); const int t = F.lane >> 2, step = 16 * jj + t, tt = d ? (SEQ - 1 - step) : step;
;                   *(u32x4*)(YD + ((size_t)d * T + (size_t)b * SEQ + tt) * 512 + hd * 64 + 32 * rb + 8 * (F.lane & 3)) = w; }
;                 cur = cur == CH_NST - 1 ? 0 : cur + 1;
.Lchain_nostore:
	v_mfma_f32_32x32x16_bf16 v[32:47], v[134:137], v[138:141], 0
	ds_read_b64 v[154:155], v213
	ds_read_b64 v[156:157], v214
	v_add_u32_e32 v215, v131, v83
	v_add_u32_e32 v216, v131, v84
	ds_read_b64 v[158:159], v215
	ds_read_b64 v[160:161], v216
	v_add_u32_e32 v215, v129, v85
	v_add_u32_e32 v216, v129, v86
	ds_read_b64 v[162:163], v215 offset:10240
	ds_read_b64 v[164:165], v216 offset:10240
	s_waitcnt lgkmcnt(9)
	v_mfma_f32_32x32x16_bf16 v[16:31], v[142:145], v[138:141], 0
	v_add_u32_e32 v215, v130, v85
	v_add_u32_e32 v216, v130, v86
	ds_read_b64 v[166:167], v215
	ds_read_b64 v[168:169], v216
	s_waitcnt lgkmcnt(10)
	v_mfma_f32_32x32x16_bf16 v[0:15], v[146:149], v[138:141], 0
	v_add_u32_e32 v215, v131, v85
	v_add_u32_e32 v216, v131, v86
	ds_read_b64 v[170:171], v215
	ds_read_b64 v[172:173], v216
	s_waitcnt lgkmcnt(10)
	v_mfma_f32_32x32x16_bf16 v[32:47], v[150:153], v[102:105], v[32:47]
	v_add_u32_e32 v215, v129, v87
	v_add_u32_e32 v216, v129, v88
	ds_read_b64 v[174:175], v215 offset:10240
	ds_read_b64 v[176:177], v216 offset:10240
	s_waitcnt lgkmcnt(10)
	v_mfma_f32_32x32x16_bf16 v[16:31], v[154:157], v[102:105], v[16:31]
	v_add_u32_e32 v215, v130, v87
	v_add_u32_e32 v216, v130, v88
	ds_read_b64 v[178:179], v215
	ds_read_b64 v[180:181], v216
	s_waitcnt lgkmcnt(10)
	v_mfma_f32_32x32x16_bf16 v[0:15], v[158:161], v[102:105], v[0:15]
	v_add_u32_e32 v215, v131, v87
	v_add_u32_e32 v216, v131, v88
	ds_read_b64 v[182:183], v215
	ds_read_b64 v[184:185], v216
	s_waitcnt lgkmcnt(10)
	v_mfma_f32_32x32x16_bf16 v[32:47], v[162:165], v[106:109], v[32:47]
	v_add_u32_e32 v215, v129, v89
	v_add_u32_e32 v216, v129, v90
	ds_read_b64 v[194:195], v215 offset:10240
	ds_read_b64 v[196:197], v216 offset:10240
	s_waitcnt lgkmcnt(10)
	v_mfma_f32_32x32x16_bf16 v[16:31], v[166:169], v[106:109], v[16:31]
	v_add_u32_e32 v215, v130, v89
	v_add_u32_e32 v216, v130, v90
	ds_read_b64 v[198:199], v215
	ds_read_b64 v[200:201], v216
	s_waitcnt lgkmcnt(10)
	v_mfma_f32_32x32x16_bf16 v[0:15], v[170:173], v[106:109], v[0:15]
	v_add_u32_e32 v215, v131, v89
	v_add_u32_e32 v216, v131, v90
	ds_read_b64 v[202:203], v215
	ds_read_b64 v[204:205], v216
	s_waitcnt lgkmcnt(10)
	v_mfma_f32_32x32x16_bf16 v[32:47], v[174:177], v[52:55], v[32:47]
	s_add_i32 s2, s5, 1
	s_cmp_lg_u32 s5, 5
	s_cselect_b32 s5, s2, 0
	s_mul_i32 s2, s5, 0x3800
	v_add3_u32 v126, s2, v78, v77
	s_waitcnt lgkmcnt(4)
	v_mfma_f32_32x32x16_bf16 v[32:47], v[194:197], v[48:51], v[32:47]
	v_add3_u32 v127, s2, v76, v77
	v_add3_u32 v128, s2, v79, v77
	v_add_u32_e32 v129, s2, v80
	v_add_u32_e32 v130, s2, v81
	v_add_u32_e32 v131, s2, v82
	v_mfma_f32_32x32x16_bf16 v[16:31], v[178:181], v[52:55], v[16:31]
	v_add_u32_e32 v132, v129, v83
	v_add_u32_e32 v212, v129, v84
	v_add_u32_e32 v213, v130, v83
	v_add_u32_e32 v214, v130, v84
	v_mfma_f32_32x32x16_bf16 v[0:15], v[182:185], v[52:55], v[0:15]
	v_add_u32_e32 v217, s4, v92
	s_add_i32 s4, s4, -16
	v_cndmask_b32_e32 v210, v217, v101, vcc
	v_ashrrev_i32_e32 v211, 31, v210
	v_lshl_add_u64 v[210:211], s[52:53], 0, v[210:211]
	s_waitcnt lgkmcnt(2)
	v_mfma_f32_32x32x16_bf16 v[16:31], v[198:201], v[48:51], v[16:31]
	v_add_u32_e32 v101, 16, v101
	v_lshlrev_b64 v[210:211], 10, v[210:211]
	v_lshl_add_u64 v[210:211], v[74:75], 0, v[210:211]
	v_add_u32_e32 v217, 0x15000, v56
	v_cvt_pk_bf16_f32 v32, v32, s0
	v_cvt_pk_bf16_f32 v33, v33, s0
	v_cvt_pk_bf16_f32 v34, v34, s0
	v_cvt_pk_bf16_f32 v35, v35, s0
	v_cvt_pk_bf16_f32 v36, v36, s0
	v_cvt_pk_bf16_f32 v37, v37, s0
	v_cvt_pk_bf16_f32 v38, v38, s0
	v_cvt_pk_bf16_f32 v39, v39, s0
	s_waitcnt lgkmcnt(0)
	v_mfma_f32_32x32x16_bf16 v[0:15], v[202:205], v[48:51], v[0:15]
	ds_write_b16 v93, v32
	ds_write_b16 v94, v33
	ds_write_b16 v95, v34
	ds_write_b16 v96, v35
	ds_write_b16 v97, v36
	ds_write_b16 v98, v37
	ds_write_b16 v99, v38
	ds_write_b16 v100, v39
	ds_read_b128 v[206:209], v217
	s_cmp_eq_u32 s4, -1
	s_cbranch_scc0 .LBB0_756
	s_waitcnt lgkmcnt(0)
	global_store_dwordx4 v[210:211], v[206:209], off
	s_waitcnt vmcnt(0)
	s_waitcnt lgkmcnt(0)
	s_mov_b64 s[4:5], 0
	s_barrier
